# v091 + uneven conv row split: workgroups 0-63 (which then run the carry) take 6 rows per wave, the other conv workgroups 15 (layer 0) / 13 (layer 1)
# speedup vs baseline: 1.0086x; 1.0043x over previous
; __device__ __forceinline__ void phase_conv(Frame& F, int l, int nblk) {
;     ...
;     const int nrows = l == 0 ? MT : ML, nwv = nblk * NWAVES, rpw = (nrows + nwv - 1) / nwv, r_lo = (F.vcu * NWAVES + F.wave) * rpw, r_hi = r_lo + rpw < nrows ? r_lo + rpw : nrows;
;     if (r_lo >= r_hi) return;
.LBB0_429:
	s_lshl_b32 s0, s14, 3
	s_abs_i32 s1, s0
	v_cvt_f32_u32_e32 v1, s1
	s_add_i32 s3, s0, 0x47ff
	s_sub_i32 s4, 0xffffb801, s0
	s_xor_b32 s0, s3, s0
	v_rcp_iflag_f32_e32 v1, v1
	s_max_i32 s3, s3, s4
	s_sub_i32 s4, 0, s1
	s_ashr_i32 s2, s13, 6
	v_mul_f32_e32 v1, 0x4f7ffffe, v1
	v_cvt_u32_f32_e32 v1, v1
	s_ashr_i32 s0, s0, 31
	v_readfirstlane_b32 s5, v1
	s_mul_i32 s4, s4, s5
	s_mul_hi_u32 s4, s5, s4
	s_add_i32 s5, s5, s4
	s_mul_hi_u32 s4, s3, s5
	s_mul_i32 s5, s4, s1
	s_sub_i32 s3, s3, s5
	s_add_i32 s6, s4, 1
	s_sub_i32 s5, s3, s1
	s_cmp_ge_u32 s3, s1
	s_cselect_b32 s4, s6, s4
	s_cselect_b32 s3, s5, s3
	s_add_i32 s5, s4, 1
	s_cmp_ge_u32 s3, s1
	s_cselect_b32 s1, s5, s4
	s_xor_b32 s1, s1, s0
	s_sub_i32 s0, s1, s0
	s_lshl_b32 s1, s12, 3
	s_add_i32 s1, s1, s2
	s_cmp_lt_u32 s1, 0x200
	s_cbranch_scc1 .Lcv0_a
	s_mov_b32 s0, 15
	s_sub_i32 s1, s1, 0x200
	s_mul_i32 s2, s0, s1
	s_add_i32 s2, s2, 3072
	s_branch .Lcv0_j
.Lcv0_a:
	s_mov_b32 s0, 6
	s_mul_i32 s2, s0, s1
; #define GAS __attribute__((address_space(1)))
; __device__ __forceinline__ void phase_conv(Frame& F, int l, int nblk) {
;     const bf16* P = WSP(bf16, WS_R1); bf16* cc = WSP(bf16, WS_R2);
;     const float* cw = F.in[I_CONVW] + (size_t)l * 3 * DCONV; const float* gn = F.in[I_ONCG] + (size_t)l * DCONV;
;     f32x4 w[3][3][2], g[3][2];
; #pragma unroll
;     for (int ch = 0; ch < 3; ++ch) { const int c0 = ch * 512 + 8 * F.lane;
; #pragma unroll
;         for (int t = 0; t < 3; ++t) { w[ch][t][0] = *(const GAS f32x4*)(cw + t * DCONV + c0); w[ch][t][1] = *(const GAS f32x4*)(cw + t * DCONV + c0 + 4); }
;         g[ch][0] = *(const GAS f32x4*)(gn + c0); g[ch][1] = *(const GAS f32x4*)(gn + c0 + 4); }
;     const int nrows = l == 0 ? MT : ML, nwv = nblk * NWAVES, rpw = (nrows + nwv - 1) / nwv, r_lo = (F.vcu * NWAVES + F.wave) * rpw, r_hi = r_lo + rpw < nrows ? r_lo + rpw : nrows;
;     if (r_lo >= r_hi) return;
;     f32x4 zp[3][2], zc[3][2], zn[3][2];
;     conv_z(P + (size_t)(r_lo > 0 ? r_lo - 1 : 0) * PROJW, F.lane, zp); conv_z(P + (size_t)r_lo * PROJW, F.lane, zc);
;     for (int r = r_lo; r < r_hi; ++r) {
;         bool hp, hn; if (r < ML) { const int x = r & 63; hp = x > 0; hn = x < 63; } else { const int t = (r - ML) & 255; hp = t > 0; hn = t < 255; }
;         const float mp = hp ? 1.f : 0.f, mn = hn ? 1.f : 0.f;
;         const bf16* p0 = P + (size_t)r * PROJW;
;         v4u braw[3];
; #pragma unroll
;         for (int ch = 0; ch < 3; ++ch) braw[ch] = *(const GAS v4u*)(p0 + ch * 512 + 8 * F.lane);
;         conv_z(P + (size_t)(r + 1 < nrows ? r + 1 : r) * PROJW, F.lane, zn);
.Lcv0_j:
	s_add_i32 s0, s2, s0
	s_min_i32 s0, s0, 0x4800
	s_cmp_ge_i32 s2, s0
	s_cbranch_scc1 .LBB0_432
	s_add_u32 s4, s38, 0x57900000
	s_load_dwordx2 s[6:7], s[96:97], 0x90
	s_load_dwordx2 s[8:9], s[96:97], 0x40
	s_addc_u32 s5, s39, 0
	s_max_i32 s1, s2, 1
	v_lshlrev_b32_e32 v1, 3, v0
	s_add_i32 s1, s1, -1
	v_and_b32_e32 v1, 0x1f8, v1
	s_mul_hi_u32 s3, s1, 0x1800
	s_mulk_i32 s1, 0x1800
	v_lshlrev_b32_e32 v110, 2, v1
	v_mov_b32_e32 v111, 0
	s_add_u32 s10, s4, s1
	s_waitcnt lgkmcnt(0)
	global_load_dwordx4 v[2:5], v110, s[6:7] offset:16
	global_load_dwordx4 v[6:9], v110, s[6:7]
	global_load_dwordx4 v[10:13], v110, s[6:7] offset:2064
	global_load_dwordx4 v[14:17], v110, s[6:7] offset:2048
	v_or_b32_e32 v66, 0x1000, v110
	v_lshl_add_u64 v[90:91], s[8:9], 0, v[110:111]
	global_load_dwordx4 v[18:21], v110, s[8:9] offset:2064
	global_load_dwordx4 v[22:25], v110, s[8:9] offset:2048
	global_load_dwordx4 v[26:29], v110, s[8:9] offset:16
	global_load_dwordx4 v[30:33], v110, s[8:9]
	s_addc_u32 s11, s5, s3
	v_lshlrev_b32_e32 v110, 1, v1
	global_load_dwordx4 v[98:101], v110, s[10:11] offset:3072
	v_mov_b32_e32 v67, v111
	s_ashr_i32 s3, s2, 31
	s_mul_i32 s16, s2, 0x1800
	v_lshl_add_u64 v[50:51], s[8:9], 0, v[66:67]
	s_movk_i32 s14, 0x3000
	v_lshl_add_u64 v[34:35], s[10:11], 0, v[110:111]
	s_mov_b64 s[12:13], 0xc00
	s_mul_hi_i32 s17, s2, 0x1800
	s_add_u32 s10, s4, s16
	v_add_co_u32_e32 v54, vcc, s14, v50
	v_lshl_add_u64 v[34:35], v[34:35], 0, s[12:13]
	s_addc_u32 s11, s5, s17
	s_movk_i32 s1, 0x1000
	v_addc_co_u32_e32 v55, vcc, 0, v51, vcc
	global_load_dwordx4 v[102:105], v[34:35], off offset:1024
	global_load_dwordx4 v[106:109], v[34:35], off offset:2048
	global_load_dwordx4 v[120:123], v110, s[10:11] offset:3072
	s_nop 0
	global_load_dwordx4 v[34:37], v66, s[6:7] offset:16
	global_load_dwordx4 v[38:41], v66, s[6:7]
	v_lshl_add_u64 v[42:43], s[10:11], 0, v[110:111]
	s_mov_b64 s[6:7], 0x3000
	v_add_co_u32_e32 v70, vcc, s1, v50
	v_lshl_add_u64 v[42:43], v[42:43], 0, s[12:13]
	v_lshl_add_u64 v[52:53], v[50:51], 0, s[6:7]
	s_mov_b64 s[10:11], 0x1800
	v_addc_co_u32_e32 v71, vcc, 0, v51, vcc
	global_load_dwordx4 v[126:129], v[42:43], off offset:1024
	global_load_dwordx4 v[134:137], v[42:43], off offset:2048
	s_nop 0
	global_load_dwordx4 v[42:45], v[54:55], off
	global_load_dwordx4 v[46:49], v[52:53], off offset:16
	v_lshl_add_u64 v[68:69], v[50:51], 0, s[10:11]
	global_load_dwordx4 v[50:53], v[70:71], off offset:2048
	global_load_dwordx4 v[54:57], v[68:69], off offset:16
	global_load_dwordx4 v[58:61], v66, s[8:9] offset:16
	global_load_dwordx4 v[62:65], v66, s[8:9]
	s_mov_b64 s[8:9], 0x3800
	v_add_co_u32_e32 v92, vcc, s14, v90
	v_lshl_add_u64 v[74:75], v[90:91], 0, s[8:9]
	s_nop 0
	v_addc_co_u32_e32 v93, vcc, 0, v91, vcc
	s_mov_b64 s[8:9], 0x2000
	v_lshl_add_u64 v[94:95], v[90:91], 0, s[8:9]
	global_load_dwordx4 v[66:69], v[74:75], off offset:16
	global_load_dwordx4 v[70:73], v[92:93], off offset:-4096
	v_lshl_add_u64 v[96:97], v[90:91], 0, s[6:7]
	global_load_dwordx4 v[74:77], v[92:93], off offset:2048
	global_load_dwordx4 v[78:81], v[92:93], off
	global_load_dwordx4 v[82:85], v[94:95], off offset:16
	global_load_dwordx4 v[86:89], v[96:97], off offset:16
	v_add_co_u32_e32 v114, vcc, s1, v90
	v_lshl_add_u64 v[112:113], v[90:91], 0, s[10:11]
	s_nop 0
	v_addc_co_u32_e32 v115, vcc, 0, v91, vcc
	global_load_dwordx4 v[90:93], v[114:115], off offset:2048
	global_load_dwordx4 v[94:97], v[112:113], off offset:16
	v_lshl_add_u64 v[112:113], s[4:5], 0, v[110:111]
	s_lshl_b64 s[4:5], s[2:3], 12
	s_add_u32 s14, s38, s4
	s_addc_u32 s15, s39, s5
	s_add_u32 s16, s38, s16
	s_mov_b32 s1, 0xffff0000
	s_addc_u32 s17, s39, s17
	s_mov_b32 s3, 0x57900000
	v_mov_b32_e32 v184, 0x358637bd
	s_mov_b32 s18, 0xf800000
	v_mov_b32_e32 v185, 0x260
	s_movk_i32 s19, 0x7fff
	s_mov_b32 s20, 0x61b00000
	v_mov_b32_e32 v186, 0x1800
	s_waitcnt vmcnt(0)
	v_lshlrev_b32_e32 v152, 16, v98
	v_and_b32_e32 v153, 0xffff0000, v98
	v_mbcnt_hi_u32_b32 v98, -1, v238
	v_lshlrev_b32_e32 v156, 16, v99
	v_and_b32_e32 v157, 0xffff0000, v99
	v_and_b32_e32 v99, 64, v98
	v_xor_b32_e32 v1, 1, v98
	v_add_u32_e32 v99, 64, v99
	v_lshlrev_b32_e32 v158, 16, v100
	v_and_b32_e32 v159, 0xffff0000, v100
	v_cmp_lt_i32_e32 vcc, v1, v99
	v_xor_b32_e32 v100, 2, v98
	v_lshlrev_b32_e32 v160, 16, v101
	v_cndmask_b32_e32 v1, v98, v1, vcc
	v_cmp_lt_i32_e32 vcc, v100, v99
	v_and_b32_e32 v161, 0xffff0000, v101
	v_lshlrev_b32_e32 v150, 16, v102
	v_cndmask_b32_e32 v100, v98, v100, vcc
	v_lshlrev_b32_e32 v165, 2, v100
	v_xor_b32_e32 v100, 4, v98
	v_cmp_lt_i32_e32 vcc, v100, v99
	v_and_b32_e32 v151, 0xffff0000, v102
	v_lshlrev_b32_e32 v154, 16, v103
	v_cndmask_b32_e32 v100, v98, v100, vcc
	v_lshlrev_b32_e32 v182, 2, v100
	v_xor_b32_e32 v100, 8, v98
	v_cmp_lt_i32_e32 vcc, v100, v99
	v_and_b32_e32 v155, 0xffff0000, v103
	v_lshlrev_b32_e32 v146, 16, v104
	v_cndmask_b32_e32 v98, v98, v100, vcc
	v_lshlrev_b32_e32 v183, 2, v98
	v_and_b32_e32 v98, 63, v0
	v_and_b32_e32 v147, 0xffff0000, v104
	v_lshlrev_b32_e32 v148, 16, v105
	v_and_b32_e32 v149, 0xffff0000, v105
	v_lshlrev_b32_e32 v142, 16, v106
	v_and_b32_e32 v143, 0xffff0000, v106
	v_lshlrev_b32_e32 v144, 16, v107
	v_and_b32_e32 v145, 0xffff0000, v107
	v_lshlrev_b32_e32 v140, 16, v108
	v_and_b32_e32 v141, 0xffff0000, v108
	v_lshlrev_b32_e32 v138, 16, v109
	v_and_b32_e32 v139, 0xffff0000, v109
	v_lshlrev_b32_e32 v116, 16, v120
	v_and_b32_e32 v117, 0xffff0000, v120
	v_lshlrev_b32_e32 v120, 16, v121
	v_and_b32_e32 v121, 0xffff0000, v121
	v_lshlrev_b32_e32 v114, 16, v122
	v_and_b32_e32 v115, 0xffff0000, v122
	v_lshlrev_b32_e32 v118, 16, v123
	v_and_b32_e32 v119, 0xffff0000, v123
	v_lshlrev_b32_e32 v122, 16, v126
	v_and_b32_e32 v123, 0xffff0000, v126
	v_lshlrev_b32_e32 v124, 16, v127
	v_and_b32_e32 v125, 0xffff0000, v127
	v_lshlrev_b32_e32 v126, 16, v128
	v_and_b32_e32 v127, 0xffff0000, v128
	v_lshlrev_b32_e32 v128, 16, v129
	v_and_b32_e32 v129, 0xffff0000, v129
	v_lshlrev_b32_e32 v130, 16, v134
	v_and_b32_e32 v131, 0xffff0000, v134
	v_lshlrev_b32_e32 v132, 16, v135
	v_and_b32_e32 v133, 0xffff0000, v135
	v_lshlrev_b32_e32 v134, 16, v136
	v_and_b32_e32 v135, 0xffff0000, v136
	v_lshlrev_b32_e32 v136, 16, v137
	v_and_b32_e32 v137, 0xffff0000, v137
	v_lshlrev_b32_e32 v1, 2, v1
	v_lshlrev_b32_e32 v110, 4, v98

; __device__ __forceinline__ void phase_conv(Frame& F, int l, int nblk) {
;     ...
;     const int nrows = l == 0 ? MT : ML, nwv = nblk * NWAVES, rpw = (nrows + nwv - 1) / nwv, r_lo = (F.vcu * NWAVES + F.wave) * rpw, r_hi = r_lo + rpw < nrows ? r_lo + rpw : nrows;
;     if (r_lo >= r_hi) return;
.LBB0_1449:
	s_lshl_b32 s0, s14, 3
	s_abs_i32 s1, s0
	v_cvt_f32_u32_e32 v1, s1
	s_add_i32 s3, s0, 0x3fff
	s_sub_i32 s4, 0xffffc001, s0
	s_xor_b32 s0, s3, s0
	v_rcp_iflag_f32_e32 v1, v1
	s_max_i32 s3, s3, s4
	s_sub_i32 s4, 0, s1
	s_ashr_i32 s2, s13, 6
	v_mul_f32_e32 v1, 0x4f7ffffe, v1
	v_cvt_u32_f32_e32 v1, v1
	s_ashr_i32 s0, s0, 31
	v_readfirstlane_b32 s5, v1
	s_mul_i32 s4, s4, s5
	s_mul_hi_u32 s4, s5, s4
	s_add_i32 s5, s5, s4
	s_mul_hi_u32 s4, s3, s5
	s_mul_i32 s5, s4, s1
	s_sub_i32 s3, s3, s5
	s_add_i32 s6, s4, 1
	s_sub_i32 s5, s3, s1
	s_cmp_ge_u32 s3, s1
	s_cselect_b32 s4, s6, s4
	s_cselect_b32 s3, s5, s3
	s_add_i32 s5, s4, 1
	s_cmp_ge_u32 s3, s1
	s_cselect_b32 s1, s5, s4
	s_xor_b32 s1, s1, s0
	s_sub_i32 s0, s1, s0
	s_lshl_b32 s1, s12, 3
	s_add_i32 s1, s1, s2
	s_cmp_lt_u32 s1, 0x200
	s_cbranch_scc1 .Lcv1_a
	s_mov_b32 s0, 13
	s_sub_i32 s1, s1, 0x200
	s_mul_i32 s2, s0, s1
	s_add_i32 s2, s2, 3072
	s_branch .Lcv1_j

; #define GAS __attribute__((address_space(1)))
; __device__ __forceinline__ void unpack8(const v4u w, f32x4& lo, f32x4& hi) { lo = (f32x4){bflo(w.x), bfhi(w.x), bflo(w.y), bfhi(w.y)}; hi = (f32x4){bflo(w.z), bfhi(w.z), bflo(w.w), bfhi(w.w)}; }
; __device__ __forceinline__ void conv_z(const bf16* prow, int lane, f32x4 (&z)[3][2]) {
; #pragma unroll
;     for (int ch = 0; ch < 3; ++ch) { const int c0 = ch * 512 + 8 * lane; const v4u zz = *(const GAS v4u*)(prow + DCONV + c0); unpack8(zz, z[ch][0], z[ch][1]); }
; __device__ __forceinline__ void phase_conv(Frame& F, int l, int nblk) {
;     ...
;     f32x4 w[3][3][2], g[3][2];
; #pragma unroll
;     for (int ch = 0; ch < 3; ++ch) { const int c0 = ch * 512 + 8 * F.lane;
; #pragma unroll
;         for (int t = 0; t < 3; ++t) { w[ch][t][0] = *(const GAS f32x4*)(cw + t * DCONV + c0); w[ch][t][1] = *(const GAS f32x4*)(cw + t * DCONV + c0 + 4); }
;         g[ch][0] = *(const GAS f32x4*)(gn + c0); g[ch][1] = *(const GAS f32x4*)(gn + c0 + 4); }
;     const int nrows = l == 0 ? MT : ML, nwv = nblk * NWAVES, rpw = (nrows + nwv - 1) / nwv, r_lo = (F.vcu * NWAVES + F.wave) * rpw, r_hi = r_lo + rpw < nrows ? r_lo + rpw : nrows;
;     if (r_lo >= r_hi) return;
;     f32x4 zp[3][2], zc[3][2], zn[3][2];
;     conv_z(P + (size_t)(r_lo > 0 ? r_lo - 1 : 0) * PROJW, F.lane, zp); conv_z(P + (size_t)r_lo * PROJW, F.lane, zc);
.Lcv1_j:
	s_add_i32 s0, s2, s0
	s_min_i32 s18, s0, 0x4000
	s_cmp_ge_i32 s2, s18
	s_cbranch_scc1 .LBB0_1452
	s_load_dwordx2 s[0:1], s[96:97], 0x90
	s_load_dwordx2 s[6:7], s[96:97], 0x40
	s_add_u32 s4, s33, 0x57900000
	s_addc_u32 s5, s40, 0
	v_lshlrev_b32_e32 v1, 3, v0
	s_waitcnt lgkmcnt(0)
	s_add_u32 s0, s0, 0x1800
	s_addc_u32 s1, s1, 0
	s_add_u32 s6, s6, 0x4800
	s_addc_u32 s7, s7, 0
	s_max_i32 s3, s2, 1
	s_add_i32 s3, s3, -1
	v_and_b32_e32 v1, 0x1f8, v1
	s_mul_hi_u32 s9, s3, 0x1800
	s_mulk_i32 s3, 0x1800
	v_lshlrev_b32_e32 v110, 2, v1
	v_mov_b32_e32 v111, 0
	s_add_u32 s8, s4, s3
	global_load_dwordx4 v[2:5], v110, s[0:1] offset:16
	global_load_dwordx4 v[6:9], v110, s[0:1]
	v_or_b32_e32 v82, 0x800, v110
	v_or_b32_e32 v58, 0x1000, v110
	v_lshl_add_u64 v[90:91], s[6:7], 0, v[110:111]
	global_load_dwordx4 v[10:13], v110, s[6:7] offset:16
	global_load_dwordx4 v[14:17], v110, s[6:7]
	s_addc_u32 s9, s5, s9
	v_lshlrev_b32_e32 v110, 1, v1
	global_load_dwordx4 v[98:101], v110, s[8:9] offset:3072
	v_mov_b32_e32 v59, v111
	v_lshl_add_u64 v[42:43], s[6:7], 0, v[58:59]
	s_movk_i32 s15, 0x3000
	v_add_co_u32_e32 v48, vcc, s15, v42
	s_movk_i32 s14, 0x1000
	s_nop 0
	v_addc_co_u32_e32 v49, vcc, 0, v43, vcc
	v_mov_b32_e32 v83, v111
	v_add_co_u32_e32 v62, vcc, s14, v42
	v_lshl_add_u64 v[66:67], s[6:7], 0, v[82:83]
	s_nop 0
	v_addc_co_u32_e32 v63, vcc, 0, v43, vcc
	v_lshl_add_u64 v[18:19], s[8:9], 0, v[110:111]
	s_mov_b64 s[12:13], 0xc00
	v_add_co_u32_e32 v70, vcc, s15, v66
	v_lshl_add_u64 v[34:35], v[18:19], 0, s[12:13]
	s_ashr_i32 s3, s2, 31
	s_mul_i32 s16, s2, 0x1800
	v_addc_co_u32_e32 v71, vcc, 0, v67, vcc
	global_load_dwordx4 v[102:105], v[34:35], off offset:1024
	global_load_dwordx4 v[18:21], v82, s[0:1] offset:16
	global_load_dwordx4 v[22:25], v82, s[0:1]
	global_load_dwordx4 v[106:109], v[34:35], off offset:2048
	global_load_dwordx4 v[26:29], v58, s[0:1] offset:16
	global_load_dwordx4 v[30:33], v58, s[0:1]
	s_mul_hi_i32 s17, s2, 0x1800
	s_add_u32 s0, s4, s16
	v_add_co_u32_e32 v86, vcc, s14, v66
	s_addc_u32 s1, s5, s17
	s_nop 0
	v_addc_co_u32_e32 v87, vcc, 0, v67, vcc
	s_mov_b64 s[8:9], 0x1800
	s_mov_b64 s[10:11], 0x3000
	v_lshl_add_u64 v[34:35], s[0:1], 0, v[110:111]
	v_add_co_u32_e32 v94, vcc, s15, v90
	v_lshl_add_u64 v[44:45], v[42:43], 0, s[10:11]
	v_lshl_add_u64 v[46:47], v[34:35], 0, s[12:13]
	v_lshl_add_u64 v[60:61], v[42:43], 0, s[8:9]
	v_lshl_add_u64 v[68:69], v[66:67], 0, s[10:11]
	v_addc_co_u32_e32 v95, vcc, 0, v91, vcc
	global_load_dwordx4 v[120:123], v110, s[0:1] offset:3072
	global_load_dwordx4 v[126:129], v[46:47], off offset:1024
	global_load_dwordx4 v[34:37], v[48:49], off
	global_load_dwordx4 v[38:41], v[44:45], off offset:16
	global_load_dwordx4 v[134:137], v[46:47], off offset:2048
	s_nop 0
	global_load_dwordx4 v[42:45], v[62:63], off offset:2048
	global_load_dwordx4 v[46:49], v[60:61], off offset:16
	global_load_dwordx4 v[50:53], v58, s[6:7] offset:16
	global_load_dwordx4 v[54:57], v58, s[6:7]
	s_nop 0
	global_load_dwordx4 v[58:61], v[70:71], off
	global_load_dwordx4 v[62:65], v[68:69], off offset:16
	v_lshl_add_u64 v[84:85], v[66:67], 0, s[8:9]
	global_load_dwordx4 v[66:69], v[86:87], off offset:2048
	global_load_dwordx4 v[70:73], v[84:85], off offset:16
	global_load_dwordx4 v[74:77], v82, s[6:7] offset:16
	global_load_dwordx4 v[78:81], v82, s[6:7]
	v_add_co_u32_e32 v114, vcc, s14, v90
	v_lshl_add_u64 v[92:93], v[90:91], 0, s[10:11]
	s_nop 0
	v_addc_co_u32_e32 v115, vcc, 0, v91, vcc
	global_load_dwordx4 v[82:85], v[94:95], off
	global_load_dwordx4 v[86:89], v[92:93], off offset:16
	v_lshl_add_u64 v[112:113], v[90:91], 0, s[8:9]
	global_load_dwordx4 v[90:93], v[114:115], off offset:2048
	global_load_dwordx4 v[94:97], v[112:113], off offset:16
	v_lshl_add_u64 v[112:113], s[4:5], 0, v[110:111]
	s_lshl_b64 s[4:5], s[2:3], 12
	s_add_u32 s14, s33, s4
	s_addc_u32 s15, s40, s5
	s_add_u32 s16, s33, s16
	s_mov_b32 s0, 0xffff0000
	s_addc_u32 s17, s40, s17
	s_mov_b32 s1, 0x57900000
	v_mov_b32_e32 v184, 0x358637bd
	s_mov_b32 s3, 0xf800000
	v_mov_b32_e32 v185, 0x260
	s_movk_i32 s19, 0x7fff
	s_mov_b32 s20, 0x61b00000
	v_mov_b32_e32 v186, 0x1800
	s_waitcnt vmcnt(0)
	v_lshlrev_b32_e32 v152, 16, v98
	v_and_b32_e32 v153, 0xffff0000, v98
	v_mbcnt_hi_u32_b32 v98, -1, v238
	v_lshlrev_b32_e32 v156, 16, v99
	v_and_b32_e32 v157, 0xffff0000, v99
	v_and_b32_e32 v99, 64, v98
	v_xor_b32_e32 v1, 1, v98
	v_add_u32_e32 v99, 64, v99
	v_lshlrev_b32_e32 v158, 16, v100
	v_and_b32_e32 v159, 0xffff0000, v100
	v_cmp_lt_i32_e32 vcc, v1, v99
	v_xor_b32_e32 v100, 2, v98
	v_lshlrev_b32_e32 v160, 16, v101
	v_cndmask_b32_e32 v1, v98, v1, vcc
	v_cmp_lt_i32_e32 vcc, v100, v99
	v_and_b32_e32 v161, 0xffff0000, v101
	v_lshlrev_b32_e32 v1, 2, v1
	v_cndmask_b32_e32 v100, v98, v100, vcc
	v_lshlrev_b32_e32 v165, 2, v100
	v_xor_b32_e32 v100, 4, v98
	v_cmp_lt_i32_e32 vcc, v100, v99
	v_lshlrev_b32_e32 v150, 16, v102
	s_nop 0
	v_cndmask_b32_e32 v100, v98, v100, vcc
	v_lshlrev_b32_e32 v182, 2, v100
	v_xor_b32_e32 v100, 8, v98
	v_cmp_lt_i32_e32 vcc, v100, v99
	v_and_b32_e32 v151, 0xffff0000, v102
	v_lshlrev_b32_e32 v154, 16, v103
	v_cndmask_b32_e32 v98, v98, v100, vcc
	v_lshlrev_b32_e32 v183, 2, v98
	v_and_b32_e32 v98, 63, v0
	v_and_b32_e32 v155, 0xffff0000, v103
	v_lshlrev_b32_e32 v146, 16, v104
	v_and_b32_e32 v147, 0xffff0000, v104
	v_lshlrev_b32_e32 v148, 16, v105
	v_and_b32_e32 v149, 0xffff0000, v105
	v_lshlrev_b32_e32 v142, 16, v106
	v_and_b32_e32 v143, 0xffff0000, v106
	v_lshlrev_b32_e32 v144, 16, v107
	v_and_b32_e32 v145, 0xffff0000, v107
	v_lshlrev_b32_e32 v140, 16, v108
	v_and_b32_e32 v141, 0xffff0000, v108
	v_lshlrev_b32_e32 v138, 16, v109
	v_and_b32_e32 v139, 0xffff0000, v109
	v_lshlrev_b32_e32 v116, 16, v120
	v_and_b32_e32 v117, 0xffff0000, v120
	v_lshlrev_b32_e32 v120, 16, v121
	v_and_b32_e32 v121, 0xffff0000, v121
	v_lshlrev_b32_e32 v114, 16, v122
	v_and_b32_e32 v115, 0xffff0000, v122
	v_lshlrev_b32_e32 v118, 16, v123
	v_and_b32_e32 v119, 0xffff0000, v123
	v_lshlrev_b32_e32 v122, 16, v126
	v_and_b32_e32 v123, 0xffff0000, v126
	v_lshlrev_b32_e32 v124, 16, v127
	v_and_b32_e32 v125, 0xffff0000, v127
	v_lshlrev_b32_e32 v126, 16, v128
	v_and_b32_e32 v127, 0xffff0000, v128
	v_lshlrev_b32_e32 v128, 16, v129
	v_and_b32_e32 v129, 0xffff0000, v129
	v_lshlrev_b32_e32 v130, 16, v134
	v_and_b32_e32 v131, 0xffff0000, v134
	v_lshlrev_b32_e32 v132, 16, v135
	v_and_b32_e32 v133, 0xffff0000, v135
	v_lshlrev_b32_e32 v134, 16, v136
	v_and_b32_e32 v135, 0xffff0000, v136
	v_lshlrev_b32_e32 v136, 16, v137
	v_and_b32_e32 v137, 0xffff0000, v137
	v_lshlrev_b32_e32 v110, 4, v98
